# MoE combine loops (both layers) rewritten by hand: coalesced lane mapping (1KB contiguous bf16 loads/stores, 512B fp8), token pipeline with TOKPOS two ahead and rows one ahead, DPP wave sum; plus fina
# baseline (speedup 1.0000x reference)
.LBB0_1683:
	s_or_b64 exec, exec, s[6:7]
	v_mov_b32_e32 v2, v0
	s_lshr_b32 s3, s95, 3
	s_waitcnt lgkmcnt(0)
	s_barrier
	s_mul_i32 s3, s3, s64
	v_readfirstlane_b32 s0, v2
	v_readlane_b32 s4, v254, 12
	s_ashr_i32 s1, s0, 6
	s_and_b32 s0, s95, 7
	s_add_i32 s3, s3, s4
	s_cmp_eq_u32 s0, 0
	s_cselect_b32 s0, s3, s2
	s_lshl_b32 s63, s0, 3
	s_add_i32 s0, s1, s63
	s_lshl_b32 s50, s95, 3
	s_cmp_lt_i32 s0, 0x10000
	s_cbranch_scc0 .LBB0_1686
	s_load_dwordx2 s[4:5], s[90:91], 0xc8
	v_and_b32_e32 v1, 63, v0
	v_lshlrev_b32_e32 v2, 4, v1
	v_lshlrev_b32_e32 v3, 3, v1
	v_mov_b32_e32 v5, 0
	v_mov_b32_e32 v6, 0x358637bd
	s_mov_b32 s16, 0x3e000000
	s_mov_b32 s17, 0
	s_waitcnt lgkmcnt(0)
	s_add_u32 s6, s4, 0xf00000
	s_addc_u32 s7, s5, 0
	s_add_u32 s8, s4, 0x1ec00000
	s_addc_u32 s9, s5, 0
	s_add_u32 s10, s4, 0x2ec00000
	s_addc_u32 s11, s5, 0
	s_add_u32 s14, s4, 0x5fc00000
	s_addc_u32 s15, s5, 0
	s_add_u32 s30, s4, 0x6bc00000
	s_addc_u32 s31, s5, 0
	s_add_i32 s1, s0, s50
	s_min_i32 s3, s0, 0xffff
	s_lshl_b32 s3, s3, 4
	s_add_u32 s34, s6, s3
	s_addc_u32 s35, s7, 0
	global_load_dwordx4 v[12:15], v5, s[34:35]
	s_min_i32 s3, s1, 0xffff
	s_lshl_b32 s3, s3, 4
	s_add_u32 s36, s6, s3
	s_addc_u32 s37, s7, 0
	global_load_dwordx4 v[16:19], v5, s[36:37]
	s_waitcnt vmcnt(1)
	v_readfirstlane_b32 s56, v12
	v_readfirstlane_b32 s57, v13
	v_readfirstlane_b32 s58, v14
	v_readfirstlane_b32 s59, v15
	s_min_i32 s3, s0, 0xffff
	s_lshl_b32 s3, s3, 11
	s_add_u32 s60, s8, s3
	s_addc_u32 s61, s9, 0
	global_load_dwordx4 v[20:23], v2, s[60:61]
	global_load_dwordx4 v[24:27], v2, s[60:61] offset:1024
	s_lshl_b32 s3, s56, 10
	s_add_u32 s68, s10, s3
	s_addc_u32 s69, s11, 0
	global_load_dwordx2 v[28:29], v3, s[68:69]
	global_load_dwordx2 v[36:37], v3, s[68:69] offset:512
	s_lshl_b32 s3, s57, 10
	s_add_u32 s72, s10, s3
	s_addc_u32 s73, s11, 0
	global_load_dwordx2 v[30:31], v3, s[72:73]
	global_load_dwordx2 v[38:39], v3, s[72:73] offset:512
	s_lshl_b32 s3, s58, 10
	s_add_u32 s74, s10, s3
	s_addc_u32 s75, s11, 0
	global_load_dwordx2 v[32:33], v3, s[74:75]
	global_load_dwordx2 v[40:41], v3, s[74:75] offset:512
	s_lshl_b32 s3, s59, 10
	s_add_u32 s78, s10, s3
	s_addc_u32 s79, s11, 0
	global_load_dwordx2 v[34:35], v3, s[78:79]
	global_load_dwordx2 v[42:43], v3, s[78:79] offset:512
	s_add_i32 s1, s0, s50
	s_add_i32 s13, s1, s50
	s_min_i32 s3, s13, 0xffff
	s_lshl_b32 s3, s3, 4
	s_add_u32 s34, s6, s3
	s_addc_u32 s35, s7, 0
	global_load_dwordx4 v[12:15], v5, s[34:35]
	s_waitcnt vmcnt(11)
	v_readfirstlane_b32 s56, v16
	v_readfirstlane_b32 s57, v17
	v_readfirstlane_b32 s58, v18
	v_readfirstlane_b32 s59, v19
	s_min_i32 s3, s1, 0xffff
	s_lshl_b32 s3, s3, 11
	s_add_u32 s60, s8, s3
	s_addc_u32 s61, s9, 0
	global_load_dwordx4 v[48:51], v2, s[60:61]
	global_load_dwordx4 v[52:55], v2, s[60:61] offset:1024
	s_lshl_b32 s3, s56, 10
	s_add_u32 s68, s10, s3
	s_addc_u32 s69, s11, 0
	global_load_dwordx2 v[56:57], v3, s[68:69]
	global_load_dwordx2 v[64:65], v3, s[68:69] offset:512
	s_lshl_b32 s3, s57, 10
	s_add_u32 s72, s10, s3
	s_addc_u32 s73, s11, 0
	global_load_dwordx2 v[58:59], v3, s[72:73]
	global_load_dwordx2 v[66:67], v3, s[72:73] offset:512
	s_lshl_b32 s3, s58, 10
	s_add_u32 s74, s10, s3
	s_addc_u32 s75, s11, 0
	global_load_dwordx2 v[60:61], v3, s[74:75]
	global_load_dwordx2 v[68:69], v3, s[74:75] offset:512
	s_lshl_b32 s3, s59, 10
	s_add_u32 s78, s10, s3
	s_addc_u32 s79, s11, 0
	global_load_dwordx2 v[62:63], v3, s[78:79]
	global_load_dwordx2 v[70:71], v3, s[78:79] offset:512
	s_waitcnt vmcnt(11)
	v_lshlrev_b32_e32 v80, 16, v20
	v_and_b32_e32 v81, 0xffff0000, v20
	v_lshlrev_b32_e32 v82, 16, v21
	v_and_b32_e32 v83, 0xffff0000, v21
	v_lshlrev_b32_e32 v84, 16, v22
	v_and_b32_e32 v85, 0xffff0000, v22
	v_lshlrev_b32_e32 v86, 16, v23
	v_and_b32_e32 v87, 0xffff0000, v23
	v_lshlrev_b32_e32 v88, 16, v24
	v_and_b32_e32 v89, 0xffff0000, v24
	v_lshlrev_b32_e32 v90, 16, v25
	v_and_b32_e32 v91, 0xffff0000, v25
	v_lshlrev_b32_e32 v92, 16, v26
	v_and_b32_e32 v93, 0xffff0000, v26
	v_lshlrev_b32_e32 v94, 16, v27
	v_and_b32_e32 v95, 0xffff0000, v27
	v_cvt_pk_f32_fp8_e32 v[96:97], v28
	v_cvt_pk_f32_fp8_sdwa v[98:99], v28 src0_sel:WORD_1
	v_cvt_pk_f32_fp8_e32 v[100:101], v29
	v_cvt_pk_f32_fp8_sdwa v[102:103], v29 src0_sel:WORD_1
	v_cvt_pk_f32_fp8_e32 v[104:105], v36
	v_cvt_pk_f32_fp8_sdwa v[106:107], v36 src0_sel:WORD_1
	v_cvt_pk_f32_fp8_e32 v[108:109], v37
	v_cvt_pk_f32_fp8_sdwa v[110:111], v37 src0_sel:WORD_1
	v_pk_fma_f32 v[80:81], v[96:97], s[16:17], v[80:81] op_sel_hi:[1,0,1]
	v_pk_fma_f32 v[82:83], v[98:99], s[16:17], v[82:83] op_sel_hi:[1,0,1]
	v_pk_fma_f32 v[84:85], v[100:101], s[16:17], v[84:85] op_sel_hi:[1,0,1]
	v_pk_fma_f32 v[86:87], v[102:103], s[16:17], v[86:87] op_sel_hi:[1,0,1]
	v_pk_fma_f32 v[88:89], v[104:105], s[16:17], v[88:89] op_sel_hi:[1,0,1]
	v_pk_fma_f32 v[90:91], v[106:107], s[16:17], v[90:91] op_sel_hi:[1,0,1]
	v_pk_fma_f32 v[92:93], v[108:109], s[16:17], v[92:93] op_sel_hi:[1,0,1]
	v_pk_fma_f32 v[94:95], v[110:111], s[16:17], v[94:95] op_sel_hi:[1,0,1]
	v_cvt_pk_f32_fp8_e32 v[96:97], v30
	v_cvt_pk_f32_fp8_sdwa v[98:99], v30 src0_sel:WORD_1
	v_cvt_pk_f32_fp8_e32 v[100:101], v31
	v_cvt_pk_f32_fp8_sdwa v[102:103], v31 src0_sel:WORD_1
	v_cvt_pk_f32_fp8_e32 v[104:105], v38
	v_cvt_pk_f32_fp8_sdwa v[106:107], v38 src0_sel:WORD_1
	v_cvt_pk_f32_fp8_e32 v[108:109], v39
	v_cvt_pk_f32_fp8_sdwa v[110:111], v39 src0_sel:WORD_1
	v_pk_fma_f32 v[80:81], v[96:97], s[16:17], v[80:81] op_sel_hi:[1,0,1]
	v_pk_fma_f32 v[82:83], v[98:99], s[16:17], v[82:83] op_sel_hi:[1,0,1]
	v_pk_fma_f32 v[84:85], v[100:101], s[16:17], v[84:85] op_sel_hi:[1,0,1]
	v_pk_fma_f32 v[86:87], v[102:103], s[16:17], v[86:87] op_sel_hi:[1,0,1]
	v_pk_fma_f32 v[88:89], v[104:105], s[16:17], v[88:89] op_sel_hi:[1,0,1]
	v_pk_fma_f32 v[90:91], v[106:107], s[16:17], v[90:91] op_sel_hi:[1,0,1]
	v_pk_fma_f32 v[92:93], v[108:109], s[16:17], v[92:93] op_sel_hi:[1,0,1]
	v_pk_fma_f32 v[94:95], v[110:111], s[16:17], v[94:95] op_sel_hi:[1,0,1]
	v_cvt_pk_f32_fp8_e32 v[96:97], v32
	v_cvt_pk_f32_fp8_sdwa v[98:99], v32 src0_sel:WORD_1
	v_cvt_pk_f32_fp8_e32 v[100:101], v33
	v_cvt_pk_f32_fp8_sdwa v[102:103], v33 src0_sel:WORD_1
	v_cvt_pk_f32_fp8_e32 v[104:105], v40
	v_cvt_pk_f32_fp8_sdwa v[106:107], v40 src0_sel:WORD_1
	v_cvt_pk_f32_fp8_e32 v[108:109], v41
	v_cvt_pk_f32_fp8_sdwa v[110:111], v41 src0_sel:WORD_1
	v_pk_fma_f32 v[80:81], v[96:97], s[16:17], v[80:81] op_sel_hi:[1,0,1]
	v_pk_fma_f32 v[82:83], v[98:99], s[16:17], v[82:83] op_sel_hi:[1,0,1]
	v_pk_fma_f32 v[84:85], v[100:101], s[16:17], v[84:85] op_sel_hi:[1,0,1]
	v_pk_fma_f32 v[86:87], v[102:103], s[16:17], v[86:87] op_sel_hi:[1,0,1]
	v_pk_fma_f32 v[88:89], v[104:105], s[16:17], v[88:89] op_sel_hi:[1,0,1]
	v_pk_fma_f32 v[90:91], v[106:107], s[16:17], v[90:91] op_sel_hi:[1,0,1]
	v_pk_fma_f32 v[92:93], v[108:109], s[16:17], v[92:93] op_sel_hi:[1,0,1]
	v_pk_fma_f32 v[94:95], v[110:111], s[16:17], v[94:95] op_sel_hi:[1,0,1]
	v_cvt_pk_f32_fp8_e32 v[96:97], v34
	v_cvt_pk_f32_fp8_sdwa v[98:99], v34 src0_sel:WORD_1
	v_cvt_pk_f32_fp8_e32 v[100:101], v35
	v_cvt_pk_f32_fp8_sdwa v[102:103], v35 src0_sel:WORD_1
	v_cvt_pk_f32_fp8_e32 v[104:105], v42
	v_cvt_pk_f32_fp8_sdwa v[106:107], v42 src0_sel:WORD_1
	v_cvt_pk_f32_fp8_e32 v[108:109], v43
	v_cvt_pk_f32_fp8_sdwa v[110:111], v43 src0_sel:WORD_1
	v_pk_fma_f32 v[80:81], v[96:97], s[16:17], v[80:81] op_sel_hi:[1,0,1]
	v_pk_fma_f32 v[82:83], v[98:99], s[16:17], v[82:83] op_sel_hi:[1,0,1]
	v_pk_fma_f32 v[84:85], v[100:101], s[16:17], v[84:85] op_sel_hi:[1,0,1]
	v_pk_fma_f32 v[86:87], v[102:103], s[16:17], v[86:87] op_sel_hi:[1,0,1]
	v_pk_fma_f32 v[88:89], v[104:105], s[16:17], v[88:89] op_sel_hi:[1,0,1]
	v_pk_fma_f32 v[90:91], v[106:107], s[16:17], v[90:91] op_sel_hi:[1,0,1]
	v_pk_fma_f32 v[92:93], v[108:109], s[16:17], v[92:93] op_sel_hi:[1,0,1]
	v_pk_fma_f32 v[94:95], v[110:111], s[16:17], v[94:95] op_sel_hi:[1,0,1]
	v_pk_mul_f32 v[116:117], v[80:81], v[80:81]
	v_pk_mul_f32 v[118:119], v[82:83], v[82:83]
	v_pk_mul_f32 v[120:121], v[84:85], v[84:85]
	v_pk_mul_f32 v[122:123], v[86:87], v[86:87]
	v_pk_mul_f32 v[124:125], v[88:89], v[88:89]
	v_pk_mul_f32 v[126:127], v[90:91], v[90:91]
	v_pk_mul_f32 v[128:129], v[92:93], v[92:93]
	v_pk_mul_f32 v[130:131], v[94:95], v[94:95]
	v_add_f32_e32 v112, v116, v117
	v_add_f32_e32 v112, v118, v112
	v_add_f32_e32 v112, v119, v112
	v_add_f32_e32 v112, v120, v112
	v_add_f32_e32 v112, v121, v112
	v_add_f32_e32 v112, v122, v112
	v_add_f32_e32 v112, v123, v112
	v_add_f32_e32 v112, v124, v112
	v_add_f32_e32 v112, v125, v112
	v_add_f32_e32 v112, v126, v112
	v_add_f32_e32 v112, v127, v112
	v_add_f32_e32 v112, v128, v112
	v_add_f32_e32 v112, v129, v112
	v_add_f32_e32 v112, v130, v112
	v_add_f32_e32 v112, v131, v112
	v_cvt_pk_bf16_f32 v132, v80, v81
	v_cvt_pk_bf16_f32 v133, v82, v83
	v_cvt_pk_bf16_f32 v134, v84, v85
	v_cvt_pk_bf16_f32 v135, v86, v87
	v_cvt_pk_bf16_f32 v136, v88, v89
	v_cvt_pk_bf16_f32 v137, v90, v91
	v_cvt_pk_bf16_f32 v138, v92, v93
	v_cvt_pk_bf16_f32 v139, v94, v95
	s_lshl_b32 s3, s0, 11
	s_add_u32 s62, s14, s3
	s_addc_u32 s65, s15, 0
	v_add_f32_dpp v112, v112, v112 quad_perm:[1,0,3,2] row_mask:0xf bank_mask:0xf
	s_mov_b32 s80, s62
	s_mov_b32 s81, s65
	v_add_f32_dpp v112, v112, v112 quad_perm:[2,3,0,1] row_mask:0xf bank_mask:0xf
	s_lshl_b32 s3, s0, 10
	s_add_u32 s82, s30, s3
	v_add_f32_dpp v112, v112, v112 row_half_mirror row_mask:0xf bank_mask:0xf
	s_addc_u32 s83, s31, 0
	s_nop 0
	v_add_f32_dpp v112, v112, v112 row_mirror row_mask:0xf bank_mask:0xf
	s_nop 1
	v_add_f32_dpp v112, v112, v112 row_bcast:15 row_mask:0xa bank_mask:0xf
	s_nop 1
	v_add_f32_dpp v112, v112, v112 row_bcast:31 row_mask:0xc bank_mask:0xf
	global_store_dwordx4 v2, v[132:135], s[80:81]
	global_store_dwordx4 v2, v[136:139], s[80:81] offset:1024
	v_readlane_b32 s41, v112, 63
	s_nop 3
	v_mov_b32_e32 v114, s41
	v_fmamk_f32 v114, v114, 0x3a800000, v6
	v_rsq_f32_e32 v114, v114
	s_nop 0
	v_mul_f32_e32 v116, v80, v114
	v_mul_f32_e32 v117, v81, v114
	v_mul_f32_e32 v118, v82, v114
	v_mul_f32_e32 v119, v83, v114
	v_mul_f32_e32 v120, v84, v114
	v_mul_f32_e32 v121, v85, v114
	v_mul_f32_e32 v122, v86, v114
	v_mul_f32_e32 v123, v87, v114
	v_mul_f32_e32 v124, v88, v114
	v_mul_f32_e32 v125, v89, v114
	v_mul_f32_e32 v126, v90, v114
	v_mul_f32_e32 v127, v91, v114
	v_mul_f32_e32 v128, v92, v114
	v_mul_f32_e32 v129, v93, v114
	v_mul_f32_e32 v130, v94, v114
	v_mul_f32_e32 v131, v95, v114
	v_cvt_pk_fp8_f32 v140, v116, v117
	v_cvt_pk_fp8_f32 v141, v120, v121
	v_cvt_pk_fp8_f32 v142, v124, v125
	v_cvt_pk_fp8_f32 v143, v128, v129
	v_cvt_pk_fp8_f32 v140, v118, v119 op_sel:[0,0,1]
	v_cvt_pk_fp8_f32 v141, v122, v123 op_sel:[0,0,1]
	v_cvt_pk_fp8_f32 v142, v126, v127 op_sel:[0,0,1]
	v_cvt_pk_fp8_f32 v143, v130, v131 op_sel:[0,0,1]
	s_nop 0
	global_store_dwordx2 v3, v[140:141], s[82:83]
	global_store_dwordx2 v3, v[142:143], s[82:83] offset:512
	s_mov_b32 s0, s1
	s_cmp_lt_i32 s0, 0x10000
	s_cbranch_scc0 .Lcmb0_done
.Lcmb0_loop:
	s_add_i32 s1, s0, s50
	s_add_i32 s13, s1, s50
	s_min_i32 s3, s13, 0xffff
	s_lshl_b32 s3, s3, 4
	s_add_u32 s36, s6, s3
	s_addc_u32 s37, s7, 0
	global_load_dwordx4 v[16:19], v5, s[36:37]
	s_waitcnt vmcnt(15)
	v_readfirstlane_b32 s56, v12
	v_readfirstlane_b32 s57, v13
	v_readfirstlane_b32 s58, v14
	v_readfirstlane_b32 s59, v15
	s_min_i32 s3, s1, 0xffff
	s_lshl_b32 s3, s3, 11
	s_add_u32 s60, s8, s3
	s_addc_u32 s61, s9, 0
	global_load_dwordx4 v[20:23], v2, s[60:61]
	global_load_dwordx4 v[24:27], v2, s[60:61] offset:1024
	s_lshl_b32 s3, s56, 10
	s_add_u32 s68, s10, s3
	s_addc_u32 s69, s11, 0
	global_load_dwordx2 v[28:29], v3, s[68:69]
	global_load_dwordx2 v[36:37], v3, s[68:69] offset:512
	s_lshl_b32 s3, s57, 10
	s_add_u32 s72, s10, s3
	s_addc_u32 s73, s11, 0
	global_load_dwordx2 v[30:31], v3, s[72:73]
	global_load_dwordx2 v[38:39], v3, s[72:73] offset:512
	s_lshl_b32 s3, s58, 10
	s_add_u32 s74, s10, s3
	s_addc_u32 s75, s11, 0
	global_load_dwordx2 v[32:33], v3, s[74:75]
	global_load_dwordx2 v[40:41], v3, s[74:75] offset:512
	s_lshl_b32 s3, s59, 10
	s_add_u32 s78, s10, s3
	s_addc_u32 s79, s11, 0
	global_load_dwordx2 v[34:35], v3, s[78:79]
	global_load_dwordx2 v[42:43], v3, s[78:79] offset:512
	s_waitcnt vmcnt(15)
	v_lshlrev_b32_e32 v80, 16, v48
	v_and_b32_e32 v81, 0xffff0000, v48
	v_lshlrev_b32_e32 v82, 16, v49
	v_and_b32_e32 v83, 0xffff0000, v49
	v_lshlrev_b32_e32 v84, 16, v50
	v_and_b32_e32 v85, 0xffff0000, v50
	v_lshlrev_b32_e32 v86, 16, v51
	v_and_b32_e32 v87, 0xffff0000, v51
	v_lshlrev_b32_e32 v88, 16, v52
	v_and_b32_e32 v89, 0xffff0000, v52
	v_lshlrev_b32_e32 v90, 16, v53
	v_and_b32_e32 v91, 0xffff0000, v53
	v_lshlrev_b32_e32 v92, 16, v54
	v_and_b32_e32 v93, 0xffff0000, v54
	v_lshlrev_b32_e32 v94, 16, v55
	v_and_b32_e32 v95, 0xffff0000, v55
	v_cvt_pk_f32_fp8_e32 v[96:97], v56
	v_cvt_pk_f32_fp8_sdwa v[98:99], v56 src0_sel:WORD_1
	v_cvt_pk_f32_fp8_e32 v[100:101], v57
	v_cvt_pk_f32_fp8_sdwa v[102:103], v57 src0_sel:WORD_1
	v_cvt_pk_f32_fp8_e32 v[104:105], v64
	v_cvt_pk_f32_fp8_sdwa v[106:107], v64 src0_sel:WORD_1
	v_cvt_pk_f32_fp8_e32 v[108:109], v65
	v_cvt_pk_f32_fp8_sdwa v[110:111], v65 src0_sel:WORD_1
	v_pk_fma_f32 v[80:81], v[96:97], s[16:17], v[80:81] op_sel_hi:[1,0,1]
	v_pk_fma_f32 v[82:83], v[98:99], s[16:17], v[82:83] op_sel_hi:[1,0,1]
	v_pk_fma_f32 v[84:85], v[100:101], s[16:17], v[84:85] op_sel_hi:[1,0,1]
	v_pk_fma_f32 v[86:87], v[102:103], s[16:17], v[86:87] op_sel_hi:[1,0,1]
	v_pk_fma_f32 v[88:89], v[104:105], s[16:17], v[88:89] op_sel_hi:[1,0,1]
	v_pk_fma_f32 v[90:91], v[106:107], s[16:17], v[90:91] op_sel_hi:[1,0,1]
	v_pk_fma_f32 v[92:93], v[108:109], s[16:17], v[92:93] op_sel_hi:[1,0,1]
	v_pk_fma_f32 v[94:95], v[110:111], s[16:17], v[94:95] op_sel_hi:[1,0,1]
	v_cvt_pk_f32_fp8_e32 v[96:97], v58
	v_cvt_pk_f32_fp8_sdwa v[98:99], v58 src0_sel:WORD_1
	v_cvt_pk_f32_fp8_e32 v[100:101], v59
	v_cvt_pk_f32_fp8_sdwa v[102:103], v59 src0_sel:WORD_1
	v_cvt_pk_f32_fp8_e32 v[104:105], v66
	v_cvt_pk_f32_fp8_sdwa v[106:107], v66 src0_sel:WORD_1
	v_cvt_pk_f32_fp8_e32 v[108:109], v67
	v_cvt_pk_f32_fp8_sdwa v[110:111], v67 src0_sel:WORD_1
	v_pk_fma_f32 v[80:81], v[96:97], s[16:17], v[80:81] op_sel_hi:[1,0,1]
	v_pk_fma_f32 v[82:83], v[98:99], s[16:17], v[82:83] op_sel_hi:[1,0,1]
	v_pk_fma_f32 v[84:85], v[100:101], s[16:17], v[84:85] op_sel_hi:[1,0,1]
	v_pk_fma_f32 v[86:87], v[102:103], s[16:17], v[86:87] op_sel_hi:[1,0,1]
	v_pk_fma_f32 v[88:89], v[104:105], s[16:17], v[88:89] op_sel_hi:[1,0,1]
	v_pk_fma_f32 v[90:91], v[106:107], s[16:17], v[90:91] op_sel_hi:[1,0,1]
	v_pk_fma_f32 v[92:93], v[108:109], s[16:17], v[92:93] op_sel_hi:[1,0,1]
	v_pk_fma_f32 v[94:95], v[110:111], s[16:17], v[94:95] op_sel_hi:[1,0,1]
	v_cvt_pk_f32_fp8_e32 v[96:97], v60
	v_cvt_pk_f32_fp8_sdwa v[98:99], v60 src0_sel:WORD_1
	v_cvt_pk_f32_fp8_e32 v[100:101], v61
	v_cvt_pk_f32_fp8_sdwa v[102:103], v61 src0_sel:WORD_1
	v_cvt_pk_f32_fp8_e32 v[104:105], v68
	v_cvt_pk_f32_fp8_sdwa v[106:107], v68 src0_sel:WORD_1
	v_cvt_pk_f32_fp8_e32 v[108:109], v69
	v_cvt_pk_f32_fp8_sdwa v[110:111], v69 src0_sel:WORD_1
	v_pk_fma_f32 v[80:81], v[96:97], s[16:17], v[80:81] op_sel_hi:[1,0,1]
	v_pk_fma_f32 v[82:83], v[98:99], s[16:17], v[82:83] op_sel_hi:[1,0,1]
	v_pk_fma_f32 v[84:85], v[100:101], s[16:17], v[84:85] op_sel_hi:[1,0,1]
	v_pk_fma_f32 v[86:87], v[102:103], s[16:17], v[86:87] op_sel_hi:[1,0,1]
	v_pk_fma_f32 v[88:89], v[104:105], s[16:17], v[88:89] op_sel_hi:[1,0,1]
	v_pk_fma_f32 v[90:91], v[106:107], s[16:17], v[90:91] op_sel_hi:[1,0,1]
	v_pk_fma_f32 v[92:93], v[108:109], s[16:17], v[92:93] op_sel_hi:[1,0,1]
	v_pk_fma_f32 v[94:95], v[110:111], s[16:17], v[94:95] op_sel_hi:[1,0,1]
	v_cvt_pk_f32_fp8_e32 v[96:97], v62
	v_cvt_pk_f32_fp8_sdwa v[98:99], v62 src0_sel:WORD_1
	v_cvt_pk_f32_fp8_e32 v[100:101], v63
	v_cvt_pk_f32_fp8_sdwa v[102:103], v63 src0_sel:WORD_1
	v_cvt_pk_f32_fp8_e32 v[104:105], v70
	v_cvt_pk_f32_fp8_sdwa v[106:107], v70 src0_sel:WORD_1
	v_cvt_pk_f32_fp8_e32 v[108:109], v71
	v_cvt_pk_f32_fp8_sdwa v[110:111], v71 src0_sel:WORD_1
	v_pk_fma_f32 v[80:81], v[96:97], s[16:17], v[80:81] op_sel_hi:[1,0,1]
	v_pk_fma_f32 v[82:83], v[98:99], s[16:17], v[82:83] op_sel_hi:[1,0,1]
	v_pk_fma_f32 v[84:85], v[100:101], s[16:17], v[84:85] op_sel_hi:[1,0,1]
	v_pk_fma_f32 v[86:87], v[102:103], s[16:17], v[86:87] op_sel_hi:[1,0,1]
	v_pk_fma_f32 v[88:89], v[104:105], s[16:17], v[88:89] op_sel_hi:[1,0,1]
	v_pk_fma_f32 v[90:91], v[106:107], s[16:17], v[90:91] op_sel_hi:[1,0,1]
	v_pk_fma_f32 v[92:93], v[108:109], s[16:17], v[92:93] op_sel_hi:[1,0,1]
	v_pk_fma_f32 v[94:95], v[110:111], s[16:17], v[94:95] op_sel_hi:[1,0,1]
	v_pk_mul_f32 v[116:117], v[80:81], v[80:81]
	v_pk_mul_f32 v[118:119], v[82:83], v[82:83]
	v_pk_mul_f32 v[120:121], v[84:85], v[84:85]
	v_pk_mul_f32 v[122:123], v[86:87], v[86:87]
	v_pk_mul_f32 v[124:125], v[88:89], v[88:89]
	v_pk_mul_f32 v[126:127], v[90:91], v[90:91]
	v_pk_mul_f32 v[128:129], v[92:93], v[92:93]
	v_pk_mul_f32 v[130:131], v[94:95], v[94:95]
	v_add_f32_e32 v112, v116, v117
	v_add_f32_e32 v112, v118, v112
	v_add_f32_e32 v112, v119, v112
	v_add_f32_e32 v112, v120, v112
	v_add_f32_e32 v112, v121, v112
	v_add_f32_e32 v112, v122, v112
	v_add_f32_e32 v112, v123, v112
	v_add_f32_e32 v112, v124, v112
	v_add_f32_e32 v112, v125, v112
	v_add_f32_e32 v112, v126, v112
	v_add_f32_e32 v112, v127, v112
	v_add_f32_e32 v112, v128, v112
	v_add_f32_e32 v112, v129, v112
	v_add_f32_e32 v112, v130, v112
	v_add_f32_e32 v112, v131, v112
	v_cvt_pk_bf16_f32 v132, v80, v81
	v_cvt_pk_bf16_f32 v133, v82, v83
	v_cvt_pk_bf16_f32 v134, v84, v85
	v_cvt_pk_bf16_f32 v135, v86, v87
	v_cvt_pk_bf16_f32 v136, v88, v89
	v_cvt_pk_bf16_f32 v137, v90, v91
	v_cvt_pk_bf16_f32 v138, v92, v93
	v_cvt_pk_bf16_f32 v139, v94, v95
	s_lshl_b32 s3, s0, 11
	s_add_u32 s62, s14, s3
	s_addc_u32 s65, s15, 0
	v_add_f32_dpp v112, v112, v112 quad_perm:[1,0,3,2] row_mask:0xf bank_mask:0xf
	s_mov_b32 s80, s62
	s_mov_b32 s81, s65
	v_add_f32_dpp v112, v112, v112 quad_perm:[2,3,0,1] row_mask:0xf bank_mask:0xf
	s_lshl_b32 s3, s0, 10
	s_add_u32 s82, s30, s3
	v_add_f32_dpp v112, v112, v112 row_half_mirror row_mask:0xf bank_mask:0xf
	s_addc_u32 s83, s31, 0
	s_nop 0
	v_add_f32_dpp v112, v112, v112 row_mirror row_mask:0xf bank_mask:0xf
	s_nop 1
	v_add_f32_dpp v112, v112, v112 row_bcast:15 row_mask:0xa bank_mask:0xf
	s_nop 1
	v_add_f32_dpp v112, v112, v112 row_bcast:31 row_mask:0xc bank_mask:0xf
	global_store_dwordx4 v2, v[132:135], s[80:81]
	global_store_dwordx4 v2, v[136:139], s[80:81] offset:1024
	v_readlane_b32 s41, v112, 63
	s_nop 3
	v_mov_b32_e32 v114, s41
	v_fmamk_f32 v114, v114, 0x3a800000, v6
	v_rsq_f32_e32 v114, v114
	s_nop 0
	v_mul_f32_e32 v116, v80, v114
	v_mul_f32_e32 v117, v81, v114
	v_mul_f32_e32 v118, v82, v114
	v_mul_f32_e32 v119, v83, v114
	v_mul_f32_e32 v120, v84, v114
	v_mul_f32_e32 v121, v85, v114
	v_mul_f32_e32 v122, v86, v114
	v_mul_f32_e32 v123, v87, v114
	v_mul_f32_e32 v124, v88, v114
	v_mul_f32_e32 v125, v89, v114
	v_mul_f32_e32 v126, v90, v114
	v_mul_f32_e32 v127, v91, v114
	v_mul_f32_e32 v128, v92, v114
	v_mul_f32_e32 v129, v93, v114
	v_mul_f32_e32 v130, v94, v114
	v_mul_f32_e32 v131, v95, v114
	v_cvt_pk_fp8_f32 v140, v116, v117
	v_cvt_pk_fp8_f32 v141, v120, v121
	v_cvt_pk_fp8_f32 v142, v124, v125
	v_cvt_pk_fp8_f32 v143, v128, v129
	v_cvt_pk_fp8_f32 v140, v118, v119 op_sel:[0,0,1]
	v_cvt_pk_fp8_f32 v141, v122, v123 op_sel:[0,0,1]
	v_cvt_pk_fp8_f32 v142, v126, v127 op_sel:[0,0,1]
	v_cvt_pk_fp8_f32 v143, v130, v131 op_sel:[0,0,1]
	s_nop 0
	global_store_dwordx2 v3, v[140:141], s[82:83]
	global_store_dwordx2 v3, v[142:143], s[82:83] offset:512
	s_mov_b32 s0, s1
	s_cmp_lt_i32 s0, 0x10000
	s_cbranch_scc0 .Lcmb0_done
	s_add_i32 s1, s0, s50
	s_add_i32 s13, s1, s50
	s_min_i32 s3, s13, 0xffff
	s_lshl_b32 s3, s3, 4
	s_add_u32 s34, s6, s3
	s_addc_u32 s35, s7, 0
	global_load_dwordx4 v[12:15], v5, s[34:35]
	s_waitcnt vmcnt(15)
	v_readfirstlane_b32 s56, v16
	v_readfirstlane_b32 s57, v17
	v_readfirstlane_b32 s58, v18
	v_readfirstlane_b32 s59, v19
	s_min_i32 s3, s1, 0xffff
	s_lshl_b32 s3, s3, 11
	s_add_u32 s60, s8, s3
	s_addc_u32 s61, s9, 0
	global_load_dwordx4 v[48:51], v2, s[60:61]
	global_load_dwordx4 v[52:55], v2, s[60:61] offset:1024
	s_lshl_b32 s3, s56, 10
	s_add_u32 s68, s10, s3
	s_addc_u32 s69, s11, 0
	global_load_dwordx2 v[56:57], v3, s[68:69]
	global_load_dwordx2 v[64:65], v3, s[68:69] offset:512
	s_lshl_b32 s3, s57, 10
	s_add_u32 s72, s10, s3
	s_addc_u32 s73, s11, 0
	global_load_dwordx2 v[58:59], v3, s[72:73]
	global_load_dwordx2 v[66:67], v3, s[72:73] offset:512
	s_lshl_b32 s3, s58, 10
	s_add_u32 s74, s10, s3
	s_addc_u32 s75, s11, 0
	global_load_dwordx2 v[60:61], v3, s[74:75]
	global_load_dwordx2 v[68:69], v3, s[74:75] offset:512
	s_lshl_b32 s3, s59, 10
	s_add_u32 s78, s10, s3
	s_addc_u32 s79, s11, 0
	global_load_dwordx2 v[62:63], v3, s[78:79]
	global_load_dwordx2 v[70:71], v3, s[78:79] offset:512
	s_waitcnt vmcnt(15)
	v_lshlrev_b32_e32 v80, 16, v20
	v_and_b32_e32 v81, 0xffff0000, v20
	v_lshlrev_b32_e32 v82, 16, v21
	v_and_b32_e32 v83, 0xffff0000, v21
	v_lshlrev_b32_e32 v84, 16, v22
	v_and_b32_e32 v85, 0xffff0000, v22
	v_lshlrev_b32_e32 v86, 16, v23
	v_and_b32_e32 v87, 0xffff0000, v23
	v_lshlrev_b32_e32 v88, 16, v24
	v_and_b32_e32 v89, 0xffff0000, v24
	v_lshlrev_b32_e32 v90, 16, v25
	v_and_b32_e32 v91, 0xffff0000, v25
	v_lshlrev_b32_e32 v92, 16, v26
	v_and_b32_e32 v93, 0xffff0000, v26
	v_lshlrev_b32_e32 v94, 16, v27
	v_and_b32_e32 v95, 0xffff0000, v27
	v_cvt_pk_f32_fp8_e32 v[96:97], v28
	v_cvt_pk_f32_fp8_sdwa v[98:99], v28 src0_sel:WORD_1
	v_cvt_pk_f32_fp8_e32 v[100:101], v29
	v_cvt_pk_f32_fp8_sdwa v[102:103], v29 src0_sel:WORD_1
	v_cvt_pk_f32_fp8_e32 v[104:105], v36
	v_cvt_pk_f32_fp8_sdwa v[106:107], v36 src0_sel:WORD_1
	v_cvt_pk_f32_fp8_e32 v[108:109], v37
	v_cvt_pk_f32_fp8_sdwa v[110:111], v37 src0_sel:WORD_1
	v_pk_fma_f32 v[80:81], v[96:97], s[16:17], v[80:81] op_sel_hi:[1,0,1]
	v_pk_fma_f32 v[82:83], v[98:99], s[16:17], v[82:83] op_sel_hi:[1,0,1]
	v_pk_fma_f32 v[84:85], v[100:101], s[16:17], v[84:85] op_sel_hi:[1,0,1]
	v_pk_fma_f32 v[86:87], v[102:103], s[16:17], v[86:87] op_sel_hi:[1,0,1]
	v_pk_fma_f32 v[88:89], v[104:105], s[16:17], v[88:89] op_sel_hi:[1,0,1]
	v_pk_fma_f32 v[90:91], v[106:107], s[16:17], v[90:91] op_sel_hi:[1,0,1]
	v_pk_fma_f32 v[92:93], v[108:109], s[16:17], v[92:93] op_sel_hi:[1,0,1]
	v_pk_fma_f32 v[94:95], v[110:111], s[16:17], v[94:95] op_sel_hi:[1,0,1]
	v_cvt_pk_f32_fp8_e32 v[96:97], v30
	v_cvt_pk_f32_fp8_sdwa v[98:99], v30 src0_sel:WORD_1
	v_cvt_pk_f32_fp8_e32 v[100:101], v31
	v_cvt_pk_f32_fp8_sdwa v[102:103], v31 src0_sel:WORD_1
	v_cvt_pk_f32_fp8_e32 v[104:105], v38
	v_cvt_pk_f32_fp8_sdwa v[106:107], v38 src0_sel:WORD_1
	v_cvt_pk_f32_fp8_e32 v[108:109], v39
	v_cvt_pk_f32_fp8_sdwa v[110:111], v39 src0_sel:WORD_1
	v_pk_fma_f32 v[80:81], v[96:97], s[16:17], v[80:81] op_sel_hi:[1,0,1]
	v_pk_fma_f32 v[82:83], v[98:99], s[16:17], v[82:83] op_sel_hi:[1,0,1]
	v_pk_fma_f32 v[84:85], v[100:101], s[16:17], v[84:85] op_sel_hi:[1,0,1]
	v_pk_fma_f32 v[86:87], v[102:103], s[16:17], v[86:87] op_sel_hi:[1,0,1]
	v_pk_fma_f32 v[88:89], v[104:105], s[16:17], v[88:89] op_sel_hi:[1,0,1]
	v_pk_fma_f32 v[90:91], v[106:107], s[16:17], v[90:91] op_sel_hi:[1,0,1]
	v_pk_fma_f32 v[92:93], v[108:109], s[16:17], v[92:93] op_sel_hi:[1,0,1]
	v_pk_fma_f32 v[94:95], v[110:111], s[16:17], v[94:95] op_sel_hi:[1,0,1]
	v_cvt_pk_f32_fp8_e32 v[96:97], v32
	v_cvt_pk_f32_fp8_sdwa v[98:99], v32 src0_sel:WORD_1
	v_cvt_pk_f32_fp8_e32 v[100:101], v33
	v_cvt_pk_f32_fp8_sdwa v[102:103], v33 src0_sel:WORD_1
	v_cvt_pk_f32_fp8_e32 v[104:105], v40
	v_cvt_pk_f32_fp8_sdwa v[106:107], v40 src0_sel:WORD_1
	v_cvt_pk_f32_fp8_e32 v[108:109], v41
	v_cvt_pk_f32_fp8_sdwa v[110:111], v41 src0_sel:WORD_1
	v_pk_fma_f32 v[80:81], v[96:97], s[16:17], v[80:81] op_sel_hi:[1,0,1]
	v_pk_fma_f32 v[82:83], v[98:99], s[16:17], v[82:83] op_sel_hi:[1,0,1]
	v_pk_fma_f32 v[84:85], v[100:101], s[16:17], v[84:85] op_sel_hi:[1,0,1]
	v_pk_fma_f32 v[86:87], v[102:103], s[16:17], v[86:87] op_sel_hi:[1,0,1]
	v_pk_fma_f32 v[88:89], v[104:105], s[16:17], v[88:89] op_sel_hi:[1,0,1]
	v_pk_fma_f32 v[90:91], v[106:107], s[16:17], v[90:91] op_sel_hi:[1,0,1]
	v_pk_fma_f32 v[92:93], v[108:109], s[16:17], v[92:93] op_sel_hi:[1,0,1]
	v_pk_fma_f32 v[94:95], v[110:111], s[16:17], v[94:95] op_sel_hi:[1,0,1]
	v_cvt_pk_f32_fp8_e32 v[96:97], v34
	v_cvt_pk_f32_fp8_sdwa v[98:99], v34 src0_sel:WORD_1
	v_cvt_pk_f32_fp8_e32 v[100:101], v35
	v_cvt_pk_f32_fp8_sdwa v[102:103], v35 src0_sel:WORD_1
	v_cvt_pk_f32_fp8_e32 v[104:105], v42
	v_cvt_pk_f32_fp8_sdwa v[106:107], v42 src0_sel:WORD_1
	v_cvt_pk_f32_fp8_e32 v[108:109], v43
	v_cvt_pk_f32_fp8_sdwa v[110:111], v43 src0_sel:WORD_1
	v_pk_fma_f32 v[80:81], v[96:97], s[16:17], v[80:81] op_sel_hi:[1,0,1]
	v_pk_fma_f32 v[82:83], v[98:99], s[16:17], v[82:83] op_sel_hi:[1,0,1]
	v_pk_fma_f32 v[84:85], v[100:101], s[16:17], v[84:85] op_sel_hi:[1,0,1]
	v_pk_fma_f32 v[86:87], v[102:103], s[16:17], v[86:87] op_sel_hi:[1,0,1]
	v_pk_fma_f32 v[88:89], v[104:105], s[16:17], v[88:89] op_sel_hi:[1,0,1]
	v_pk_fma_f32 v[90:91], v[106:107], s[16:17], v[90:91] op_sel_hi:[1,0,1]
	v_pk_fma_f32 v[92:93], v[108:109], s[16:17], v[92:93] op_sel_hi:[1,0,1]
	v_pk_fma_f32 v[94:95], v[110:111], s[16:17], v[94:95] op_sel_hi:[1,0,1]
	v_pk_mul_f32 v[116:117], v[80:81], v[80:81]
	v_pk_mul_f32 v[118:119], v[82:83], v[82:83]
	v_pk_mul_f32 v[120:121], v[84:85], v[84:85]
	v_pk_mul_f32 v[122:123], v[86:87], v[86:87]
	v_pk_mul_f32 v[124:125], v[88:89], v[88:89]
	v_pk_mul_f32 v[126:127], v[90:91], v[90:91]
	v_pk_mul_f32 v[128:129], v[92:93], v[92:93]
	v_pk_mul_f32 v[130:131], v[94:95], v[94:95]
	v_add_f32_e32 v112, v116, v117
	v_add_f32_e32 v112, v118, v112
	v_add_f32_e32 v112, v119, v112
	v_add_f32_e32 v112, v120, v112
	v_add_f32_e32 v112, v121, v112
	v_add_f32_e32 v112, v122, v112
	v_add_f32_e32 v112, v123, v112
	v_add_f32_e32 v112, v124, v112
	v_add_f32_e32 v112, v125, v112
	v_add_f32_e32 v112, v126, v112
	v_add_f32_e32 v112, v127, v112
	v_add_f32_e32 v112, v128, v112
	v_add_f32_e32 v112, v129, v112
	v_add_f32_e32 v112, v130, v112
	v_add_f32_e32 v112, v131, v112
	v_cvt_pk_bf16_f32 v132, v80, v81
	v_cvt_pk_bf16_f32 v133, v82, v83
	v_cvt_pk_bf16_f32 v134, v84, v85
	v_cvt_pk_bf16_f32 v135, v86, v87
	v_cvt_pk_bf16_f32 v136, v88, v89
	v_cvt_pk_bf16_f32 v137, v90, v91
	v_cvt_pk_bf16_f32 v138, v92, v93
	v_cvt_pk_bf16_f32 v139, v94, v95
	s_lshl_b32 s3, s0, 11
	s_add_u32 s62, s14, s3
	s_addc_u32 s65, s15, 0
	v_add_f32_dpp v112, v112, v112 quad_perm:[1,0,3,2] row_mask:0xf bank_mask:0xf
	s_mov_b32 s80, s62
	s_mov_b32 s81, s65
	v_add_f32_dpp v112, v112, v112 quad_perm:[2,3,0,1] row_mask:0xf bank_mask:0xf
	s_lshl_b32 s3, s0, 10
	s_add_u32 s82, s30, s3
	v_add_f32_dpp v112, v112, v112 row_half_mirror row_mask:0xf bank_mask:0xf
	s_addc_u32 s83, s31, 0
	s_nop 0
	v_add_f32_dpp v112, v112, v112 row_mirror row_mask:0xf bank_mask:0xf
	s_nop 1
	v_add_f32_dpp v112, v112, v112 row_bcast:15 row_mask:0xa bank_mask:0xf
	s_nop 1
	v_add_f32_dpp v112, v112, v112 row_bcast:31 row_mask:0xc bank_mask:0xf
	global_store_dwordx4 v2, v[132:135], s[80:81]
	global_store_dwordx4 v2, v[136:139], s[80:81] offset:1024
	v_readlane_b32 s41, v112, 63
	s_nop 3
	v_mov_b32_e32 v114, s41
	v_fmamk_f32 v114, v114, 0x3a800000, v6
	v_rsq_f32_e32 v114, v114
	s_nop 0
	v_mul_f32_e32 v116, v80, v114
	v_mul_f32_e32 v117, v81, v114
	v_mul_f32_e32 v118, v82, v114
	v_mul_f32_e32 v119, v83, v114
	v_mul_f32_e32 v120, v84, v114
	v_mul_f32_e32 v121, v85, v114
	v_mul_f32_e32 v122, v86, v114
	v_mul_f32_e32 v123, v87, v114
	v_mul_f32_e32 v124, v88, v114
	v_mul_f32_e32 v125, v89, v114
	v_mul_f32_e32 v126, v90, v114
	v_mul_f32_e32 v127, v91, v114
	v_mul_f32_e32 v128, v92, v114
	v_mul_f32_e32 v129, v93, v114
	v_mul_f32_e32 v130, v94, v114
	v_mul_f32_e32 v131, v95, v114
	v_cvt_pk_fp8_f32 v140, v116, v117
	v_cvt_pk_fp8_f32 v141, v120, v121
	v_cvt_pk_fp8_f32 v142, v124, v125
	v_cvt_pk_fp8_f32 v143, v128, v129
	v_cvt_pk_fp8_f32 v140, v118, v119 op_sel:[0,0,1]
	v_cvt_pk_fp8_f32 v141, v122, v123 op_sel:[0,0,1]
	v_cvt_pk_fp8_f32 v142, v126, v127 op_sel:[0,0,1]
	v_cvt_pk_fp8_f32 v143, v130, v131 op_sel:[0,0,1]
	s_nop 0
	global_store_dwordx2 v3, v[140:141], s[82:83]
	global_store_dwordx2 v3, v[142:143], s[82:83] offset:512
	s_mov_b32 s0, s1
	s_cmp_lt_i32 s0, 0x10000
	s_cbranch_scc0 .Lcmb0_done
	s_branch .Lcmb0_loop
.Lcmb0_done:
	s_ashr_i32 s51, s50, 31
	s_lshl_b64 s[12:13], s[50:51], 10
	v_mov_b32_e32 v11, 0

.LBB0_3485:
	s_or_b64 exec, exec, s[8:9]
	v_mov_b32_e32 v2, v0
	s_waitcnt lgkmcnt(0)
	s_barrier
	s_nop 0
	v_readfirstlane_b32 s0, v2
	s_ashr_i32 s1, s0, 6
	s_add_i32 s0, s1, s33
	s_cmp_lt_i32 s0, 0x10000
	s_cbranch_scc0 .LBB0_3488
	s_load_dwordx2 s[4:5], s[90:91], 0xc8
	v_and_b32_e32 v1, 63, v0
	v_lshlrev_b32_e32 v2, 4, v1
	v_lshlrev_b32_e32 v3, 3, v1
	v_mov_b32_e32 v5, 0
	v_mov_b32_e32 v6, 0x358637bd
	s_mov_b32 s16, 0x3e000000
	s_mov_b32 s17, 0
	s_waitcnt lgkmcnt(0)
	s_add_u32 s6, s4, 0xf00000
	s_addc_u32 s7, s5, 0
	s_add_u32 s8, s4, 0x1ec00000
	s_addc_u32 s9, s5, 0
	s_add_u32 s10, s4, 0x2ec00000
	s_addc_u32 s11, s5, 0
	s_add_u32 s14, s4, 0x5fc00000
	s_addc_u32 s15, s5, 0
	s_add_u32 s30, s4, 0x6bc00000
	s_addc_u32 s31, s5, 0
	s_add_i32 s1, s0, s54
	s_min_i32 s3, s0, 0xffff
	s_lshl_b32 s3, s3, 4
	s_add_u32 s34, s6, s3
	s_addc_u32 s35, s7, 0
	global_load_dwordx4 v[12:15], v5, s[34:35]
	s_min_i32 s3, s1, 0xffff
	s_lshl_b32 s3, s3, 4
	s_add_u32 s36, s6, s3
	s_addc_u32 s37, s7, 0
	global_load_dwordx4 v[16:19], v5, s[36:37]
	s_waitcnt vmcnt(1)
	v_readfirstlane_b32 s56, v12
	v_readfirstlane_b32 s57, v13
	v_readfirstlane_b32 s58, v14
	v_readfirstlane_b32 s59, v15
	s_min_i32 s3, s0, 0xffff
	s_lshl_b32 s3, s3, 11
	s_add_u32 s60, s8, s3
	s_addc_u32 s61, s9, 0
	global_load_dwordx4 v[20:23], v2, s[60:61]
	global_load_dwordx4 v[24:27], v2, s[60:61] offset:1024
	s_lshl_b32 s3, s56, 10
	s_add_u32 s68, s10, s3
	s_addc_u32 s69, s11, 0
	global_load_dwordx2 v[28:29], v3, s[68:69]
	global_load_dwordx2 v[36:37], v3, s[68:69] offset:512
	s_lshl_b32 s3, s57, 10
	s_add_u32 s72, s10, s3
	s_addc_u32 s73, s11, 0
	global_load_dwordx2 v[30:31], v3, s[72:73]
	global_load_dwordx2 v[38:39], v3, s[72:73] offset:512
	s_lshl_b32 s3, s58, 10
	s_add_u32 s74, s10, s3
	s_addc_u32 s75, s11, 0
	global_load_dwordx2 v[32:33], v3, s[74:75]
	global_load_dwordx2 v[40:41], v3, s[74:75] offset:512
	s_lshl_b32 s3, s59, 10
	s_add_u32 s78, s10, s3
	s_addc_u32 s79, s11, 0
	global_load_dwordx2 v[34:35], v3, s[78:79]
	global_load_dwordx2 v[42:43], v3, s[78:79] offset:512
	s_add_i32 s1, s0, s54
	s_add_i32 s13, s1, s54
	s_min_i32 s3, s13, 0xffff
	s_lshl_b32 s3, s3, 4
	s_add_u32 s34, s6, s3
	s_addc_u32 s35, s7, 0
	global_load_dwordx4 v[12:15], v5, s[34:35]
	s_waitcnt vmcnt(11)
	v_readfirstlane_b32 s56, v16
	v_readfirstlane_b32 s57, v17
	v_readfirstlane_b32 s58, v18
	v_readfirstlane_b32 s59, v19
	s_min_i32 s3, s1, 0xffff
	s_lshl_b32 s3, s3, 11
	s_add_u32 s60, s8, s3
	s_addc_u32 s61, s9, 0
	global_load_dwordx4 v[48:51], v2, s[60:61]
	global_load_dwordx4 v[52:55], v2, s[60:61] offset:1024
	s_lshl_b32 s3, s56, 10
	s_add_u32 s68, s10, s3
	s_addc_u32 s69, s11, 0
	global_load_dwordx2 v[56:57], v3, s[68:69]
	global_load_dwordx2 v[64:65], v3, s[68:69] offset:512
	s_lshl_b32 s3, s57, 10
	s_add_u32 s72, s10, s3
	s_addc_u32 s73, s11, 0
	global_load_dwordx2 v[58:59], v3, s[72:73]
	global_load_dwordx2 v[66:67], v3, s[72:73] offset:512
	s_lshl_b32 s3, s58, 10
	s_add_u32 s74, s10, s3
	s_addc_u32 s75, s11, 0
	global_load_dwordx2 v[60:61], v3, s[74:75]
	global_load_dwordx2 v[68:69], v3, s[74:75] offset:512
	s_lshl_b32 s3, s59, 10
	s_add_u32 s78, s10, s3
	s_addc_u32 s79, s11, 0
	global_load_dwordx2 v[62:63], v3, s[78:79]
	global_load_dwordx2 v[70:71], v3, s[78:79] offset:512
	s_waitcnt vmcnt(11)
	v_lshlrev_b32_e32 v80, 16, v20
	v_and_b32_e32 v81, 0xffff0000, v20
	v_lshlrev_b32_e32 v82, 16, v21
	v_and_b32_e32 v83, 0xffff0000, v21
	v_lshlrev_b32_e32 v84, 16, v22
	v_and_b32_e32 v85, 0xffff0000, v22
	v_lshlrev_b32_e32 v86, 16, v23
	v_and_b32_e32 v87, 0xffff0000, v23
	v_lshlrev_b32_e32 v88, 16, v24
	v_and_b32_e32 v89, 0xffff0000, v24
	v_lshlrev_b32_e32 v90, 16, v25
	v_and_b32_e32 v91, 0xffff0000, v25
	v_lshlrev_b32_e32 v92, 16, v26
	v_and_b32_e32 v93, 0xffff0000, v26
	v_lshlrev_b32_e32 v94, 16, v27
	v_and_b32_e32 v95, 0xffff0000, v27
	v_cvt_pk_f32_fp8_e32 v[96:97], v28
	v_cvt_pk_f32_fp8_sdwa v[98:99], v28 src0_sel:WORD_1
	v_cvt_pk_f32_fp8_e32 v[100:101], v29
	v_cvt_pk_f32_fp8_sdwa v[102:103], v29 src0_sel:WORD_1
	v_cvt_pk_f32_fp8_e32 v[104:105], v36
	v_cvt_pk_f32_fp8_sdwa v[106:107], v36 src0_sel:WORD_1
	v_cvt_pk_f32_fp8_e32 v[108:109], v37
	v_cvt_pk_f32_fp8_sdwa v[110:111], v37 src0_sel:WORD_1
	v_pk_fma_f32 v[80:81], v[96:97], s[16:17], v[80:81] op_sel_hi:[1,0,1]
	v_pk_fma_f32 v[82:83], v[98:99], s[16:17], v[82:83] op_sel_hi:[1,0,1]
	v_pk_fma_f32 v[84:85], v[100:101], s[16:17], v[84:85] op_sel_hi:[1,0,1]
	v_pk_fma_f32 v[86:87], v[102:103], s[16:17], v[86:87] op_sel_hi:[1,0,1]
	v_pk_fma_f32 v[88:89], v[104:105], s[16:17], v[88:89] op_sel_hi:[1,0,1]
	v_pk_fma_f32 v[90:91], v[106:107], s[16:17], v[90:91] op_sel_hi:[1,0,1]
	v_pk_fma_f32 v[92:93], v[108:109], s[16:17], v[92:93] op_sel_hi:[1,0,1]
	v_pk_fma_f32 v[94:95], v[110:111], s[16:17], v[94:95] op_sel_hi:[1,0,1]
	v_cvt_pk_f32_fp8_e32 v[96:97], v30
	v_cvt_pk_f32_fp8_sdwa v[98:99], v30 src0_sel:WORD_1
	v_cvt_pk_f32_fp8_e32 v[100:101], v31
	v_cvt_pk_f32_fp8_sdwa v[102:103], v31 src0_sel:WORD_1
	v_cvt_pk_f32_fp8_e32 v[104:105], v38
	v_cvt_pk_f32_fp8_sdwa v[106:107], v38 src0_sel:WORD_1
	v_cvt_pk_f32_fp8_e32 v[108:109], v39
	v_cvt_pk_f32_fp8_sdwa v[110:111], v39 src0_sel:WORD_1
	v_pk_fma_f32 v[80:81], v[96:97], s[16:17], v[80:81] op_sel_hi:[1,0,1]
	v_pk_fma_f32 v[82:83], v[98:99], s[16:17], v[82:83] op_sel_hi:[1,0,1]
	v_pk_fma_f32 v[84:85], v[100:101], s[16:17], v[84:85] op_sel_hi:[1,0,1]
	v_pk_fma_f32 v[86:87], v[102:103], s[16:17], v[86:87] op_sel_hi:[1,0,1]
	v_pk_fma_f32 v[88:89], v[104:105], s[16:17], v[88:89] op_sel_hi:[1,0,1]
	v_pk_fma_f32 v[90:91], v[106:107], s[16:17], v[90:91] op_sel_hi:[1,0,1]
	v_pk_fma_f32 v[92:93], v[108:109], s[16:17], v[92:93] op_sel_hi:[1,0,1]
	v_pk_fma_f32 v[94:95], v[110:111], s[16:17], v[94:95] op_sel_hi:[1,0,1]
	v_cvt_pk_f32_fp8_e32 v[96:97], v32
	v_cvt_pk_f32_fp8_sdwa v[98:99], v32 src0_sel:WORD_1
	v_cvt_pk_f32_fp8_e32 v[100:101], v33
	v_cvt_pk_f32_fp8_sdwa v[102:103], v33 src0_sel:WORD_1
	v_cvt_pk_f32_fp8_e32 v[104:105], v40
	v_cvt_pk_f32_fp8_sdwa v[106:107], v40 src0_sel:WORD_1
	v_cvt_pk_f32_fp8_e32 v[108:109], v41
	v_cvt_pk_f32_fp8_sdwa v[110:111], v41 src0_sel:WORD_1
	v_pk_fma_f32 v[80:81], v[96:97], s[16:17], v[80:81] op_sel_hi:[1,0,1]
	v_pk_fma_f32 v[82:83], v[98:99], s[16:17], v[82:83] op_sel_hi:[1,0,1]
	v_pk_fma_f32 v[84:85], v[100:101], s[16:17], v[84:85] op_sel_hi:[1,0,1]
	v_pk_fma_f32 v[86:87], v[102:103], s[16:17], v[86:87] op_sel_hi:[1,0,1]
	v_pk_fma_f32 v[88:89], v[104:105], s[16:17], v[88:89] op_sel_hi:[1,0,1]
	v_pk_fma_f32 v[90:91], v[106:107], s[16:17], v[90:91] op_sel_hi:[1,0,1]
	v_pk_fma_f32 v[92:93], v[108:109], s[16:17], v[92:93] op_sel_hi:[1,0,1]
	v_pk_fma_f32 v[94:95], v[110:111], s[16:17], v[94:95] op_sel_hi:[1,0,1]
	v_cvt_pk_f32_fp8_e32 v[96:97], v34
	v_cvt_pk_f32_fp8_sdwa v[98:99], v34 src0_sel:WORD_1
	v_cvt_pk_f32_fp8_e32 v[100:101], v35
	v_cvt_pk_f32_fp8_sdwa v[102:103], v35 src0_sel:WORD_1
	v_cvt_pk_f32_fp8_e32 v[104:105], v42
	v_cvt_pk_f32_fp8_sdwa v[106:107], v42 src0_sel:WORD_1
	v_cvt_pk_f32_fp8_e32 v[108:109], v43
	v_cvt_pk_f32_fp8_sdwa v[110:111], v43 src0_sel:WORD_1
	v_pk_fma_f32 v[80:81], v[96:97], s[16:17], v[80:81] op_sel_hi:[1,0,1]
	v_pk_fma_f32 v[82:83], v[98:99], s[16:17], v[82:83] op_sel_hi:[1,0,1]
	v_pk_fma_f32 v[84:85], v[100:101], s[16:17], v[84:85] op_sel_hi:[1,0,1]
	v_pk_fma_f32 v[86:87], v[102:103], s[16:17], v[86:87] op_sel_hi:[1,0,1]
	v_pk_fma_f32 v[88:89], v[104:105], s[16:17], v[88:89] op_sel_hi:[1,0,1]
	v_pk_fma_f32 v[90:91], v[106:107], s[16:17], v[90:91] op_sel_hi:[1,0,1]
	v_pk_fma_f32 v[92:93], v[108:109], s[16:17], v[92:93] op_sel_hi:[1,0,1]
	v_pk_fma_f32 v[94:95], v[110:111], s[16:17], v[94:95] op_sel_hi:[1,0,1]
	v_pk_mul_f32 v[116:117], v[80:81], v[80:81]
	v_pk_mul_f32 v[118:119], v[82:83], v[82:83]
	v_pk_mul_f32 v[120:121], v[84:85], v[84:85]
	v_pk_mul_f32 v[122:123], v[86:87], v[86:87]
	v_pk_mul_f32 v[124:125], v[88:89], v[88:89]
	v_pk_mul_f32 v[126:127], v[90:91], v[90:91]
	v_pk_mul_f32 v[128:129], v[92:93], v[92:93]
	v_pk_mul_f32 v[130:131], v[94:95], v[94:95]
	v_add_f32_e32 v112, v116, v117
	v_add_f32_e32 v112, v118, v112
	v_add_f32_e32 v112, v119, v112
	v_add_f32_e32 v112, v120, v112
	v_add_f32_e32 v112, v121, v112
	v_add_f32_e32 v112, v122, v112
	v_add_f32_e32 v112, v123, v112
	v_add_f32_e32 v112, v124, v112
	v_add_f32_e32 v112, v125, v112
	v_add_f32_e32 v112, v126, v112
	v_add_f32_e32 v112, v127, v112
	v_add_f32_e32 v112, v128, v112
	v_add_f32_e32 v112, v129, v112
	v_add_f32_e32 v112, v130, v112
	v_add_f32_e32 v112, v131, v112
	v_cvt_pk_bf16_f32 v132, v80, v81
	v_cvt_pk_bf16_f32 v133, v82, v83
	v_cvt_pk_bf16_f32 v134, v84, v85
	v_cvt_pk_bf16_f32 v135, v86, v87
	v_cvt_pk_bf16_f32 v136, v88, v89
	v_cvt_pk_bf16_f32 v137, v90, v91
	v_cvt_pk_bf16_f32 v138, v92, v93
	v_cvt_pk_bf16_f32 v139, v94, v95
	s_lshl_b32 s3, s0, 11
	s_add_u32 s62, s14, s3
	s_addc_u32 s65, s15, 0
	v_add_f32_dpp v112, v112, v112 quad_perm:[1,0,3,2] row_mask:0xf bank_mask:0xf
	s_mov_b32 s80, s62
	s_mov_b32 s81, s65
	v_add_f32_dpp v112, v112, v112 quad_perm:[2,3,0,1] row_mask:0xf bank_mask:0xf
	s_lshl_b32 s3, s0, 10
	s_add_u32 s82, s30, s3
	v_add_f32_dpp v112, v112, v112 row_half_mirror row_mask:0xf bank_mask:0xf
	s_addc_u32 s83, s31, 0
	s_nop 0
	v_add_f32_dpp v112, v112, v112 row_mirror row_mask:0xf bank_mask:0xf
	s_nop 1
	v_add_f32_dpp v112, v112, v112 row_bcast:15 row_mask:0xa bank_mask:0xf
	s_nop 1
	v_add_f32_dpp v112, v112, v112 row_bcast:31 row_mask:0xc bank_mask:0xf
	global_store_dwordx4 v2, v[132:135], s[80:81]
	global_store_dwordx4 v2, v[136:139], s[80:81] offset:1024
	v_readlane_b32 s41, v112, 63
	s_nop 3
	v_mov_b32_e32 v114, s41
	v_fmamk_f32 v114, v114, 0x3a800000, v6
	v_rsq_f32_e32 v114, v114
	s_nop 0
	v_mul_f32_e32 v116, v80, v114
	v_mul_f32_e32 v117, v81, v114
	v_mul_f32_e32 v118, v82, v114
	v_mul_f32_e32 v119, v83, v114
	v_mul_f32_e32 v120, v84, v114
	v_mul_f32_e32 v121, v85, v114
	v_mul_f32_e32 v122, v86, v114
	v_mul_f32_e32 v123, v87, v114
	v_mul_f32_e32 v124, v88, v114
	v_mul_f32_e32 v125, v89, v114
	v_mul_f32_e32 v126, v90, v114
	v_mul_f32_e32 v127, v91, v114
	v_mul_f32_e32 v128, v92, v114
	v_mul_f32_e32 v129, v93, v114
	v_mul_f32_e32 v130, v94, v114
	v_mul_f32_e32 v131, v95, v114
	v_cvt_pk_fp8_f32 v140, v116, v117
	v_cvt_pk_fp8_f32 v141, v120, v121
	v_cvt_pk_fp8_f32 v142, v124, v125
	v_cvt_pk_fp8_f32 v143, v128, v129
	v_cvt_pk_fp8_f32 v140, v118, v119 op_sel:[0,0,1]
	v_cvt_pk_fp8_f32 v141, v122, v123 op_sel:[0,0,1]
	v_cvt_pk_fp8_f32 v142, v126, v127 op_sel:[0,0,1]
	v_cvt_pk_fp8_f32 v143, v130, v131 op_sel:[0,0,1]
	s_nop 0
	global_store_dwordx2 v3, v[140:141], s[82:83]
	global_store_dwordx2 v3, v[142:143], s[82:83] offset:512
	s_mov_b32 s0, s1
	s_cmp_lt_i32 s0, 0x10000
	s_cbranch_scc0 .Lcmb1_done
.Lcmb1_loop:
	s_add_i32 s1, s0, s54
	s_add_i32 s13, s1, s54
	s_min_i32 s3, s13, 0xffff
	s_lshl_b32 s3, s3, 4
	s_add_u32 s36, s6, s3
	s_addc_u32 s37, s7, 0
	global_load_dwordx4 v[16:19], v5, s[36:37]
	s_waitcnt vmcnt(15)
	v_readfirstlane_b32 s56, v12
	v_readfirstlane_b32 s57, v13
	v_readfirstlane_b32 s58, v14
	v_readfirstlane_b32 s59, v15
	s_min_i32 s3, s1, 0xffff
	s_lshl_b32 s3, s3, 11
	s_add_u32 s60, s8, s3
	s_addc_u32 s61, s9, 0
	global_load_dwordx4 v[20:23], v2, s[60:61]
	global_load_dwordx4 v[24:27], v2, s[60:61] offset:1024
	s_lshl_b32 s3, s56, 10
	s_add_u32 s68, s10, s3
	s_addc_u32 s69, s11, 0
	global_load_dwordx2 v[28:29], v3, s[68:69]
	global_load_dwordx2 v[36:37], v3, s[68:69] offset:512
	s_lshl_b32 s3, s57, 10
	s_add_u32 s72, s10, s3
	s_addc_u32 s73, s11, 0
	global_load_dwordx2 v[30:31], v3, s[72:73]
	global_load_dwordx2 v[38:39], v3, s[72:73] offset:512
	s_lshl_b32 s3, s58, 10
	s_add_u32 s74, s10, s3
	s_addc_u32 s75, s11, 0
	global_load_dwordx2 v[32:33], v3, s[74:75]
	global_load_dwordx2 v[40:41], v3, s[74:75] offset:512
	s_lshl_b32 s3, s59, 10
	s_add_u32 s78, s10, s3
	s_addc_u32 s79, s11, 0
	global_load_dwordx2 v[34:35], v3, s[78:79]
	global_load_dwordx2 v[42:43], v3, s[78:79] offset:512
	s_waitcnt vmcnt(15)
	v_lshlrev_b32_e32 v80, 16, v48
	v_and_b32_e32 v81, 0xffff0000, v48
	v_lshlrev_b32_e32 v82, 16, v49
	v_and_b32_e32 v83, 0xffff0000, v49
	v_lshlrev_b32_e32 v84, 16, v50
	v_and_b32_e32 v85, 0xffff0000, v50
	v_lshlrev_b32_e32 v86, 16, v51
	v_and_b32_e32 v87, 0xffff0000, v51
	v_lshlrev_b32_e32 v88, 16, v52
	v_and_b32_e32 v89, 0xffff0000, v52
	v_lshlrev_b32_e32 v90, 16, v53
	v_and_b32_e32 v91, 0xffff0000, v53
	v_lshlrev_b32_e32 v92, 16, v54
	v_and_b32_e32 v93, 0xffff0000, v54
	v_lshlrev_b32_e32 v94, 16, v55
	v_and_b32_e32 v95, 0xffff0000, v55
	v_cvt_pk_f32_fp8_e32 v[96:97], v56
	v_cvt_pk_f32_fp8_sdwa v[98:99], v56 src0_sel:WORD_1
	v_cvt_pk_f32_fp8_e32 v[100:101], v57
	v_cvt_pk_f32_fp8_sdwa v[102:103], v57 src0_sel:WORD_1
	v_cvt_pk_f32_fp8_e32 v[104:105], v64
	v_cvt_pk_f32_fp8_sdwa v[106:107], v64 src0_sel:WORD_1
	v_cvt_pk_f32_fp8_e32 v[108:109], v65
	v_cvt_pk_f32_fp8_sdwa v[110:111], v65 src0_sel:WORD_1
	v_pk_fma_f32 v[80:81], v[96:97], s[16:17], v[80:81] op_sel_hi:[1,0,1]
	v_pk_fma_f32 v[82:83], v[98:99], s[16:17], v[82:83] op_sel_hi:[1,0,1]
	v_pk_fma_f32 v[84:85], v[100:101], s[16:17], v[84:85] op_sel_hi:[1,0,1]
	v_pk_fma_f32 v[86:87], v[102:103], s[16:17], v[86:87] op_sel_hi:[1,0,1]
	v_pk_fma_f32 v[88:89], v[104:105], s[16:17], v[88:89] op_sel_hi:[1,0,1]
	v_pk_fma_f32 v[90:91], v[106:107], s[16:17], v[90:91] op_sel_hi:[1,0,1]
	v_pk_fma_f32 v[92:93], v[108:109], s[16:17], v[92:93] op_sel_hi:[1,0,1]
	v_pk_fma_f32 v[94:95], v[110:111], s[16:17], v[94:95] op_sel_hi:[1,0,1]
	v_cvt_pk_f32_fp8_e32 v[96:97], v58
	v_cvt_pk_f32_fp8_sdwa v[98:99], v58 src0_sel:WORD_1
	v_cvt_pk_f32_fp8_e32 v[100:101], v59
	v_cvt_pk_f32_fp8_sdwa v[102:103], v59 src0_sel:WORD_1
	v_cvt_pk_f32_fp8_e32 v[104:105], v66
	v_cvt_pk_f32_fp8_sdwa v[106:107], v66 src0_sel:WORD_1
	v_cvt_pk_f32_fp8_e32 v[108:109], v67
	v_cvt_pk_f32_fp8_sdwa v[110:111], v67 src0_sel:WORD_1
	v_pk_fma_f32 v[80:81], v[96:97], s[16:17], v[80:81] op_sel_hi:[1,0,1]
	v_pk_fma_f32 v[82:83], v[98:99], s[16:17], v[82:83] op_sel_hi:[1,0,1]
	v_pk_fma_f32 v[84:85], v[100:101], s[16:17], v[84:85] op_sel_hi:[1,0,1]
	v_pk_fma_f32 v[86:87], v[102:103], s[16:17], v[86:87] op_sel_hi:[1,0,1]
	v_pk_fma_f32 v[88:89], v[104:105], s[16:17], v[88:89] op_sel_hi:[1,0,1]
	v_pk_fma_f32 v[90:91], v[106:107], s[16:17], v[90:91] op_sel_hi:[1,0,1]
	v_pk_fma_f32 v[92:93], v[108:109], s[16:17], v[92:93] op_sel_hi:[1,0,1]
	v_pk_fma_f32 v[94:95], v[110:111], s[16:17], v[94:95] op_sel_hi:[1,0,1]
	v_cvt_pk_f32_fp8_e32 v[96:97], v60
	v_cvt_pk_f32_fp8_sdwa v[98:99], v60 src0_sel:WORD_1
	v_cvt_pk_f32_fp8_e32 v[100:101], v61
	v_cvt_pk_f32_fp8_sdwa v[102:103], v61 src0_sel:WORD_1
	v_cvt_pk_f32_fp8_e32 v[104:105], v68
	v_cvt_pk_f32_fp8_sdwa v[106:107], v68 src0_sel:WORD_1
	v_cvt_pk_f32_fp8_e32 v[108:109], v69
	v_cvt_pk_f32_fp8_sdwa v[110:111], v69 src0_sel:WORD_1
	v_pk_fma_f32 v[80:81], v[96:97], s[16:17], v[80:81] op_sel_hi:[1,0,1]
	v_pk_fma_f32 v[82:83], v[98:99], s[16:17], v[82:83] op_sel_hi:[1,0,1]
	v_pk_fma_f32 v[84:85], v[100:101], s[16:17], v[84:85] op_sel_hi:[1,0,1]
	v_pk_fma_f32 v[86:87], v[102:103], s[16:17], v[86:87] op_sel_hi:[1,0,1]
	v_pk_fma_f32 v[88:89], v[104:105], s[16:17], v[88:89] op_sel_hi:[1,0,1]
	v_pk_fma_f32 v[90:91], v[106:107], s[16:17], v[90:91] op_sel_hi:[1,0,1]
	v_pk_fma_f32 v[92:93], v[108:109], s[16:17], v[92:93] op_sel_hi:[1,0,1]
	v_pk_fma_f32 v[94:95], v[110:111], s[16:17], v[94:95] op_sel_hi:[1,0,1]
	v_cvt_pk_f32_fp8_e32 v[96:97], v62
	v_cvt_pk_f32_fp8_sdwa v[98:99], v62 src0_sel:WORD_1
	v_cvt_pk_f32_fp8_e32 v[100:101], v63
	v_cvt_pk_f32_fp8_sdwa v[102:103], v63 src0_sel:WORD_1
	v_cvt_pk_f32_fp8_e32 v[104:105], v70
	v_cvt_pk_f32_fp8_sdwa v[106:107], v70 src0_sel:WORD_1
	v_cvt_pk_f32_fp8_e32 v[108:109], v71
	v_cvt_pk_f32_fp8_sdwa v[110:111], v71 src0_sel:WORD_1
	v_pk_fma_f32 v[80:81], v[96:97], s[16:17], v[80:81] op_sel_hi:[1,0,1]
	v_pk_fma_f32 v[82:83], v[98:99], s[16:17], v[82:83] op_sel_hi:[1,0,1]
	v_pk_fma_f32 v[84:85], v[100:101], s[16:17], v[84:85] op_sel_hi:[1,0,1]
	v_pk_fma_f32 v[86:87], v[102:103], s[16:17], v[86:87] op_sel_hi:[1,0,1]
	v_pk_fma_f32 v[88:89], v[104:105], s[16:17], v[88:89] op_sel_hi:[1,0,1]
	v_pk_fma_f32 v[90:91], v[106:107], s[16:17], v[90:91] op_sel_hi:[1,0,1]
	v_pk_fma_f32 v[92:93], v[108:109], s[16:17], v[92:93] op_sel_hi:[1,0,1]
	v_pk_fma_f32 v[94:95], v[110:111], s[16:17], v[94:95] op_sel_hi:[1,0,1]
	v_pk_mul_f32 v[116:117], v[80:81], v[80:81]
	v_pk_mul_f32 v[118:119], v[82:83], v[82:83]
	v_pk_mul_f32 v[120:121], v[84:85], v[84:85]
	v_pk_mul_f32 v[122:123], v[86:87], v[86:87]
	v_pk_mul_f32 v[124:125], v[88:89], v[88:89]
	v_pk_mul_f32 v[126:127], v[90:91], v[90:91]
	v_pk_mul_f32 v[128:129], v[92:93], v[92:93]
	v_pk_mul_f32 v[130:131], v[94:95], v[94:95]
	v_add_f32_e32 v112, v116, v117
	v_add_f32_e32 v112, v118, v112
	v_add_f32_e32 v112, v119, v112
	v_add_f32_e32 v112, v120, v112
	v_add_f32_e32 v112, v121, v112
	v_add_f32_e32 v112, v122, v112
	v_add_f32_e32 v112, v123, v112
	v_add_f32_e32 v112, v124, v112
	v_add_f32_e32 v112, v125, v112
	v_add_f32_e32 v112, v126, v112
	v_add_f32_e32 v112, v127, v112
	v_add_f32_e32 v112, v128, v112
	v_add_f32_e32 v112, v129, v112
	v_add_f32_e32 v112, v130, v112
	v_add_f32_e32 v112, v131, v112
	v_cvt_pk_bf16_f32 v132, v80, v81
	v_cvt_pk_bf16_f32 v133, v82, v83
	v_cvt_pk_bf16_f32 v134, v84, v85
	v_cvt_pk_bf16_f32 v135, v86, v87
	v_cvt_pk_bf16_f32 v136, v88, v89
	v_cvt_pk_bf16_f32 v137, v90, v91
	v_cvt_pk_bf16_f32 v138, v92, v93
	v_cvt_pk_bf16_f32 v139, v94, v95
	s_lshl_b32 s3, s0, 11
	s_add_u32 s62, s14, s3
	s_addc_u32 s65, s15, 0
	v_add_f32_dpp v112, v112, v112 quad_perm:[1,0,3,2] row_mask:0xf bank_mask:0xf
	s_mov_b32 s80, s62
	s_mov_b32 s81, s65
	v_add_f32_dpp v112, v112, v112 quad_perm:[2,3,0,1] row_mask:0xf bank_mask:0xf
	s_lshl_b32 s3, s0, 10
	s_add_u32 s82, s30, s3
	v_add_f32_dpp v112, v112, v112 row_half_mirror row_mask:0xf bank_mask:0xf
	s_addc_u32 s83, s31, 0
	s_nop 0
	v_add_f32_dpp v112, v112, v112 row_mirror row_mask:0xf bank_mask:0xf
	s_nop 1
	v_add_f32_dpp v112, v112, v112 row_bcast:15 row_mask:0xa bank_mask:0xf
	s_nop 1
	v_add_f32_dpp v112, v112, v112 row_bcast:31 row_mask:0xc bank_mask:0xf
	global_store_dwordx4 v2, v[132:135], s[80:81]
	global_store_dwordx4 v2, v[136:139], s[80:81] offset:1024
	v_readlane_b32 s41, v112, 63
	s_nop 3
	v_mov_b32_e32 v114, s41
	v_fmamk_f32 v114, v114, 0x3a800000, v6
	v_rsq_f32_e32 v114, v114
	s_nop 0
	v_mul_f32_e32 v116, v80, v114
	v_mul_f32_e32 v117, v81, v114
	v_mul_f32_e32 v118, v82, v114
	v_mul_f32_e32 v119, v83, v114
	v_mul_f32_e32 v120, v84, v114
	v_mul_f32_e32 v121, v85, v114
	v_mul_f32_e32 v122, v86, v114
	v_mul_f32_e32 v123, v87, v114
	v_mul_f32_e32 v124, v88, v114
	v_mul_f32_e32 v125, v89, v114
	v_mul_f32_e32 v126, v90, v114
	v_mul_f32_e32 v127, v91, v114
	v_mul_f32_e32 v128, v92, v114
	v_mul_f32_e32 v129, v93, v114
	v_mul_f32_e32 v130, v94, v114
	v_mul_f32_e32 v131, v95, v114
	v_cvt_pk_fp8_f32 v140, v116, v117
	v_cvt_pk_fp8_f32 v141, v120, v121
	v_cvt_pk_fp8_f32 v142, v124, v125
	v_cvt_pk_fp8_f32 v143, v128, v129
	v_cvt_pk_fp8_f32 v140, v118, v119 op_sel:[0,0,1]
	v_cvt_pk_fp8_f32 v141, v122, v123 op_sel:[0,0,1]
	v_cvt_pk_fp8_f32 v142, v126, v127 op_sel:[0,0,1]
	v_cvt_pk_fp8_f32 v143, v130, v131 op_sel:[0,0,1]
	s_nop 0
	global_store_dwordx2 v3, v[140:141], s[82:83]
	global_store_dwordx2 v3, v[142:143], s[82:83] offset:512
	s_mov_b32 s0, s1
	s_cmp_lt_i32 s0, 0x10000
	s_cbranch_scc0 .Lcmb1_done
	s_add_i32 s1, s0, s54
	s_add_i32 s13, s1, s54
	s_min_i32 s3, s13, 0xffff
	s_lshl_b32 s3, s3, 4
	s_add_u32 s34, s6, s3
	s_addc_u32 s35, s7, 0
	global_load_dwordx4 v[12:15], v5, s[34:35]
	s_waitcnt vmcnt(15)
	v_readfirstlane_b32 s56, v16
	v_readfirstlane_b32 s57, v17
	v_readfirstlane_b32 s58, v18
	v_readfirstlane_b32 s59, v19
	s_min_i32 s3, s1, 0xffff
	s_lshl_b32 s3, s3, 11
	s_add_u32 s60, s8, s3
	s_addc_u32 s61, s9, 0
	global_load_dwordx4 v[48:51], v2, s[60:61]
	global_load_dwordx4 v[52:55], v2, s[60:61] offset:1024
	s_lshl_b32 s3, s56, 10
	s_add_u32 s68, s10, s3
	s_addc_u32 s69, s11, 0
	global_load_dwordx2 v[56:57], v3, s[68:69]
	global_load_dwordx2 v[64:65], v3, s[68:69] offset:512
	s_lshl_b32 s3, s57, 10
	s_add_u32 s72, s10, s3
	s_addc_u32 s73, s11, 0
	global_load_dwordx2 v[58:59], v3, s[72:73]
	global_load_dwordx2 v[66:67], v3, s[72:73] offset:512
	s_lshl_b32 s3, s58, 10
	s_add_u32 s74, s10, s3
	s_addc_u32 s75, s11, 0
	global_load_dwordx2 v[60:61], v3, s[74:75]
	global_load_dwordx2 v[68:69], v3, s[74:75] offset:512
	s_lshl_b32 s3, s59, 10
	s_add_u32 s78, s10, s3
	s_addc_u32 s79, s11, 0
	global_load_dwordx2 v[62:63], v3, s[78:79]
	global_load_dwordx2 v[70:71], v3, s[78:79] offset:512
	s_waitcnt vmcnt(15)
	v_lshlrev_b32_e32 v80, 16, v20
	v_and_b32_e32 v81, 0xffff0000, v20
	v_lshlrev_b32_e32 v82, 16, v21
	v_and_b32_e32 v83, 0xffff0000, v21
	v_lshlrev_b32_e32 v84, 16, v22
	v_and_b32_e32 v85, 0xffff0000, v22
	v_lshlrev_b32_e32 v86, 16, v23
	v_and_b32_e32 v87, 0xffff0000, v23
	v_lshlrev_b32_e32 v88, 16, v24
	v_and_b32_e32 v89, 0xffff0000, v24
	v_lshlrev_b32_e32 v90, 16, v25
	v_and_b32_e32 v91, 0xffff0000, v25
	v_lshlrev_b32_e32 v92, 16, v26
	v_and_b32_e32 v93, 0xffff0000, v26
	v_lshlrev_b32_e32 v94, 16, v27
	v_and_b32_e32 v95, 0xffff0000, v27
	v_cvt_pk_f32_fp8_e32 v[96:97], v28
	v_cvt_pk_f32_fp8_sdwa v[98:99], v28 src0_sel:WORD_1
	v_cvt_pk_f32_fp8_e32 v[100:101], v29
	v_cvt_pk_f32_fp8_sdwa v[102:103], v29 src0_sel:WORD_1
	v_cvt_pk_f32_fp8_e32 v[104:105], v36
	v_cvt_pk_f32_fp8_sdwa v[106:107], v36 src0_sel:WORD_1
	v_cvt_pk_f32_fp8_e32 v[108:109], v37
	v_cvt_pk_f32_fp8_sdwa v[110:111], v37 src0_sel:WORD_1
	v_pk_fma_f32 v[80:81], v[96:97], s[16:17], v[80:81] op_sel_hi:[1,0,1]
	v_pk_fma_f32 v[82:83], v[98:99], s[16:17], v[82:83] op_sel_hi:[1,0,1]
	v_pk_fma_f32 v[84:85], v[100:101], s[16:17], v[84:85] op_sel_hi:[1,0,1]
	v_pk_fma_f32 v[86:87], v[102:103], s[16:17], v[86:87] op_sel_hi:[1,0,1]
	v_pk_fma_f32 v[88:89], v[104:105], s[16:17], v[88:89] op_sel_hi:[1,0,1]
	v_pk_fma_f32 v[90:91], v[106:107], s[16:17], v[90:91] op_sel_hi:[1,0,1]
	v_pk_fma_f32 v[92:93], v[108:109], s[16:17], v[92:93] op_sel_hi:[1,0,1]
	v_pk_fma_f32 v[94:95], v[110:111], s[16:17], v[94:95] op_sel_hi:[1,0,1]
	v_cvt_pk_f32_fp8_e32 v[96:97], v30
	v_cvt_pk_f32_fp8_sdwa v[98:99], v30 src0_sel:WORD_1
	v_cvt_pk_f32_fp8_e32 v[100:101], v31
	v_cvt_pk_f32_fp8_sdwa v[102:103], v31 src0_sel:WORD_1
	v_cvt_pk_f32_fp8_e32 v[104:105], v38
	v_cvt_pk_f32_fp8_sdwa v[106:107], v38 src0_sel:WORD_1
	v_cvt_pk_f32_fp8_e32 v[108:109], v39
	v_cvt_pk_f32_fp8_sdwa v[110:111], v39 src0_sel:WORD_1
	v_pk_fma_f32 v[80:81], v[96:97], s[16:17], v[80:81] op_sel_hi:[1,0,1]
	v_pk_fma_f32 v[82:83], v[98:99], s[16:17], v[82:83] op_sel_hi:[1,0,1]
	v_pk_fma_f32 v[84:85], v[100:101], s[16:17], v[84:85] op_sel_hi:[1,0,1]
	v_pk_fma_f32 v[86:87], v[102:103], s[16:17], v[86:87] op_sel_hi:[1,0,1]
	v_pk_fma_f32 v[88:89], v[104:105], s[16:17], v[88:89] op_sel_hi:[1,0,1]
	v_pk_fma_f32 v[90:91], v[106:107], s[16:17], v[90:91] op_sel_hi:[1,0,1]
	v_pk_fma_f32 v[92:93], v[108:109], s[16:17], v[92:93] op_sel_hi:[1,0,1]
	v_pk_fma_f32 v[94:95], v[110:111], s[16:17], v[94:95] op_sel_hi:[1,0,1]
	v_cvt_pk_f32_fp8_e32 v[96:97], v32
	v_cvt_pk_f32_fp8_sdwa v[98:99], v32 src0_sel:WORD_1
	v_cvt_pk_f32_fp8_e32 v[100:101], v33
	v_cvt_pk_f32_fp8_sdwa v[102:103], v33 src0_sel:WORD_1
	v_cvt_pk_f32_fp8_e32 v[104:105], v40
	v_cvt_pk_f32_fp8_sdwa v[106:107], v40 src0_sel:WORD_1
	v_cvt_pk_f32_fp8_e32 v[108:109], v41
	v_cvt_pk_f32_fp8_sdwa v[110:111], v41 src0_sel:WORD_1
	v_pk_fma_f32 v[80:81], v[96:97], s[16:17], v[80:81] op_sel_hi:[1,0,1]
	v_pk_fma_f32 v[82:83], v[98:99], s[16:17], v[82:83] op_sel_hi:[1,0,1]
	v_pk_fma_f32 v[84:85], v[100:101], s[16:17], v[84:85] op_sel_hi:[1,0,1]
	v_pk_fma_f32 v[86:87], v[102:103], s[16:17], v[86:87] op_sel_hi:[1,0,1]
	v_pk_fma_f32 v[88:89], v[104:105], s[16:17], v[88:89] op_sel_hi:[1,0,1]
	v_pk_fma_f32 v[90:91], v[106:107], s[16:17], v[90:91] op_sel_hi:[1,0,1]
	v_pk_fma_f32 v[92:93], v[108:109], s[16:17], v[92:93] op_sel_hi:[1,0,1]
	v_pk_fma_f32 v[94:95], v[110:111], s[16:17], v[94:95] op_sel_hi:[1,0,1]
	v_cvt_pk_f32_fp8_e32 v[96:97], v34
	v_cvt_pk_f32_fp8_sdwa v[98:99], v34 src0_sel:WORD_1
	v_cvt_pk_f32_fp8_e32 v[100:101], v35
	v_cvt_pk_f32_fp8_sdwa v[102:103], v35 src0_sel:WORD_1
	v_cvt_pk_f32_fp8_e32 v[104:105], v42
	v_cvt_pk_f32_fp8_sdwa v[106:107], v42 src0_sel:WORD_1
	v_cvt_pk_f32_fp8_e32 v[108:109], v43
	v_cvt_pk_f32_fp8_sdwa v[110:111], v43 src0_sel:WORD_1
	v_pk_fma_f32 v[80:81], v[96:97], s[16:17], v[80:81] op_sel_hi:[1,0,1]
	v_pk_fma_f32 v[82:83], v[98:99], s[16:17], v[82:83] op_sel_hi:[1,0,1]
	v_pk_fma_f32 v[84:85], v[100:101], s[16:17], v[84:85] op_sel_hi:[1,0,1]
	v_pk_fma_f32 v[86:87], v[102:103], s[16:17], v[86:87] op_sel_hi:[1,0,1]
	v_pk_fma_f32 v[88:89], v[104:105], s[16:17], v[88:89] op_sel_hi:[1,0,1]
	v_pk_fma_f32 v[90:91], v[106:107], s[16:17], v[90:91] op_sel_hi:[1,0,1]
	v_pk_fma_f32 v[92:93], v[108:109], s[16:17], v[92:93] op_sel_hi:[1,0,1]
	v_pk_fma_f32 v[94:95], v[110:111], s[16:17], v[94:95] op_sel_hi:[1,0,1]
	v_pk_mul_f32 v[116:117], v[80:81], v[80:81]
	v_pk_mul_f32 v[118:119], v[82:83], v[82:83]
	v_pk_mul_f32 v[120:121], v[84:85], v[84:85]
	v_pk_mul_f32 v[122:123], v[86:87], v[86:87]
	v_pk_mul_f32 v[124:125], v[88:89], v[88:89]
	v_pk_mul_f32 v[126:127], v[90:91], v[90:91]
	v_pk_mul_f32 v[128:129], v[92:93], v[92:93]
	v_pk_mul_f32 v[130:131], v[94:95], v[94:95]
	v_add_f32_e32 v112, v116, v117
	v_add_f32_e32 v112, v118, v112
	v_add_f32_e32 v112, v119, v112
	v_add_f32_e32 v112, v120, v112
	v_add_f32_e32 v112, v121, v112
	v_add_f32_e32 v112, v122, v112
	v_add_f32_e32 v112, v123, v112
	v_add_f32_e32 v112, v124, v112
	v_add_f32_e32 v112, v125, v112
	v_add_f32_e32 v112, v126, v112
	v_add_f32_e32 v112, v127, v112
	v_add_f32_e32 v112, v128, v112
	v_add_f32_e32 v112, v129, v112
	v_add_f32_e32 v112, v130, v112
	v_add_f32_e32 v112, v131, v112
	v_cvt_pk_bf16_f32 v132, v80, v81
	v_cvt_pk_bf16_f32 v133, v82, v83
	v_cvt_pk_bf16_f32 v134, v84, v85
	v_cvt_pk_bf16_f32 v135, v86, v87
	v_cvt_pk_bf16_f32 v136, v88, v89
	v_cvt_pk_bf16_f32 v137, v90, v91
	v_cvt_pk_bf16_f32 v138, v92, v93
	v_cvt_pk_bf16_f32 v139, v94, v95
	s_lshl_b32 s3, s0, 11
	s_add_u32 s62, s14, s3
	s_addc_u32 s65, s15, 0
	v_add_f32_dpp v112, v112, v112 quad_perm:[1,0,3,2] row_mask:0xf bank_mask:0xf
	s_mov_b32 s80, s62
	s_mov_b32 s81, s65
	v_add_f32_dpp v112, v112, v112 quad_perm:[2,3,0,1] row_mask:0xf bank_mask:0xf
	s_lshl_b32 s3, s0, 10
	s_add_u32 s82, s30, s3
	v_add_f32_dpp v112, v112, v112 row_half_mirror row_mask:0xf bank_mask:0xf
	s_addc_u32 s83, s31, 0
	s_nop 0
	v_add_f32_dpp v112, v112, v112 row_mirror row_mask:0xf bank_mask:0xf
	s_nop 1
	v_add_f32_dpp v112, v112, v112 row_bcast:15 row_mask:0xa bank_mask:0xf
	s_nop 1
	v_add_f32_dpp v112, v112, v112 row_bcast:31 row_mask:0xc bank_mask:0xf
	global_store_dwordx4 v2, v[132:135], s[80:81]
	global_store_dwordx4 v2, v[136:139], s[80:81] offset:1024
	v_readlane_b32 s41, v112, 63
	s_nop 3
	v_mov_b32_e32 v114, s41
	v_fmamk_f32 v114, v114, 0x3a800000, v6
	v_rsq_f32_e32 v114, v114
	s_nop 0
	v_mul_f32_e32 v116, v80, v114
	v_mul_f32_e32 v117, v81, v114
	v_mul_f32_e32 v118, v82, v114
	v_mul_f32_e32 v119, v83, v114
	v_mul_f32_e32 v120, v84, v114
	v_mul_f32_e32 v121, v85, v114
	v_mul_f32_e32 v122, v86, v114
	v_mul_f32_e32 v123, v87, v114
	v_mul_f32_e32 v124, v88, v114
	v_mul_f32_e32 v125, v89, v114
	v_mul_f32_e32 v126, v90, v114
	v_mul_f32_e32 v127, v91, v114
	v_mul_f32_e32 v128, v92, v114
	v_mul_f32_e32 v129, v93, v114
	v_mul_f32_e32 v130, v94, v114
	v_mul_f32_e32 v131, v95, v114
	v_cvt_pk_fp8_f32 v140, v116, v117
	v_cvt_pk_fp8_f32 v141, v120, v121
	v_cvt_pk_fp8_f32 v142, v124, v125
	v_cvt_pk_fp8_f32 v143, v128, v129
	v_cvt_pk_fp8_f32 v140, v118, v119 op_sel:[0,0,1]
	v_cvt_pk_fp8_f32 v141, v122, v123 op_sel:[0,0,1]
	v_cvt_pk_fp8_f32 v142, v126, v127 op_sel:[0,0,1]
	v_cvt_pk_fp8_f32 v143, v130, v131 op_sel:[0,0,1]
	s_nop 0
	global_store_dwordx2 v3, v[140:141], s[82:83]
	global_store_dwordx2 v3, v[142:143], s[82:83] offset:512
	s_mov_b32 s0, s1
	s_cmp_lt_i32 s0, 0x10000
	s_cbranch_scc0 .Lcmb1_done
	s_branch .Lcmb1_loop
.Lcmb1_done:
	v_mov_b32_e32 v11, 0
